# P0 RMSNorm tasks: norm_mix gain vectors loaded once before the task loop (no load + vmcnt(0) between the row stores), on top of the combine-phase changes
# speedup vs baseline: 1.0159x; 1.0159x over previous
.LBB0_18:
	s_or_b64 exec, exec, s[0:1]
	s_ashr_i32 s5, s5, 31
	s_ashr_i32 s4, s4, 31
	s_mov_b64 s[0:1], exec
	v_readlane_b32 s8, v255, 12
	v_readlane_b32 s9, v255, 13
	s_and_b64 s[8:9], s[0:1], s[8:9]
	s_mov_b64 exec, s[8:9]
	s_add_i32 s7, 0, 0x20280
	v_mov_b32_e32 v2, 0
	v_mov_b32_e32 v3, v2
	v_mov_b32_e32 v4, s7
	ds_write_b64 v4, v[2:3]
	s_or_b64 exec, exec, s[0:1]
	s_mul_i32 s1, s6, s2
	s_sub_i32 s1, s3, s1
	s_xor_b32 s0, s5, s4
	s_add_i32 s3, s6, 1
	s_sub_i32 s4, s1, s2
	s_cmp_ge_u32 s1, s2
	s_cselect_b32 s3, s3, s6
	s_cselect_b32 s1, s4, s1
	s_add_i32 s4, s3, 1
	s_cmp_ge_u32 s1, s2
	s_cselect_b32 s1, s4, s3
	s_xor_b32 s1, s1, s0
	s_sub_i32 s35, s1, s0
	s_cmp_gt_i32 s35, 0
	s_cselect_b64 s[76:77], -1, 0
	s_cmp_gt_i32 s34, 0
	s_cselect_b64 s[78:79], -1, 0
	s_or_b64 s[0:1], s[78:79], s[76:77]
	s_mov_b32 s23, 0
	s_andn2_b64 vcc, exec, s[0:1]
	s_waitcnt lgkmcnt(0)
	s_barrier
	s_cbranch_vccnz .LBB0_219
	v_readlane_b32 s0, v255, 18
	s_mulk_i32 s0, 0x2100
	v_lshrrev_b32_e32 v98, 3, v1
	v_and_b32_e32 v4, 7, v0
	s_add_i32 s0, s0, 0
	v_readlane_b32 s2, v255, 8
	v_mul_u32_u24_e32 v3, 0x84, v98
	v_lshlrev_b32_e32 v5, 4, v4
	s_cmpk_lt_u32 s10, 0x100
	s_mul_i32 s1, s2, s35
	v_add3_u32 v99, s0, v3, v5
	v_lshlrev_b32_e32 v102, 3, v4
	v_mul_u32_u24_e32 v3, 0x420, v4
	v_lshlrev_b32_e32 v4, 2, v98
	s_cselect_b64 s[80:81], -1, 0
	s_lshl_b32 s66, s1, 2
	v_mov_b32_e32 v101, 0
	v_lshlrev_b32_e32 v2, 2, v0
	v_add3_u32 v105, s0, v3, v4
	v_lshlrev_b32_e32 v100, 4, v1
	v_readlane_b32 s0, v255, 14
	v_and_b32_e32 v2, 28, v2
	v_lshl_add_u64 v[110:111], s[14:15], 0, v[100:101]
	global_load_dwordx4 v[140:143], v[110:111], off
	global_load_dwordx4 v[144:147], v[110:111], off offset:1024
	global_load_dwordx4 v[148:151], v[110:111], off offset:2048
	global_load_dwordx4 v[152:155], v[110:111], off offset:3072
	v_lshl_add_u64 v[112:113], s[12:13], 0, v[100:101]
	v_lshlrev_b32_e32 v100, 2, v1
	v_readlane_b32 s1, v255, 15
	s_add_u32 s82, s90, 0xe00400
	v_cmp_eq_u32_e64 s[6:7], 0, v1
	v_lshl_add_u64 v[114:115], s[0:1], 0, v[100:101]
	v_lshlrev_b32_e32 v100, 2, v2
	v_mbcnt_lo_u32_b32 v2, -1, 0
	s_mul_i32 s67, s33, s2
	s_addc_u32 s83, s91, 0
	v_mov_b32_e32 v103, v101
	v_or_b32_e32 v104, 8, v98
	v_or_b32_e32 v106, 16, v98
	v_or_b32_e32 v108, 24, v98
	s_add_i32 s90, 0, 0x20284
	s_add_i32 s91, 0, 0x20280
	v_mov_b32_e32 v107, 0x3727c5ac
	s_mov_b32 s92, 0xf800000
	v_mov_b32_e32 v109, 0x260
	v_mbcnt_hi_u32_b32 v116, -1, v2
	s_branch .LBB0_23

.LBB0_151:
	s_or_b64 exec, exec, s[0:1]
	v_readfirstlane_b32 s2, v2
	s_cmp_ge_i32 s2, s35
	s_mov_b64 s[0:1], 0
	s_cbranch_scc1 .LBB0_155
	s_lshl_b32 s0, s2, 2
	s_add_i32 s60, s0, s66
	s_cmpk_gt_i32 s60, 0x3fff
	s_cbranch_scc1 .LBB0_154
	s_ashr_i32 s61, s60, 31
	s_lshl_b64 s[0:1], s[60:61], 12
	v_lshl_add_u64 v[2:3], v[112:113], 0, s[0:1]
	global_load_dwordx4 v[42:45], v[2:3], off nt
	global_load_dwordx4 v[30:33], v[2:3], off offset:1024 nt
	global_load_dwordx4 v[18:21], v[2:3], off offset:2048 nt
	global_load_dwordx4 v[6:9], v[2:3], off offset:3072 nt
	s_or_b32 s28, s60, 1
	s_ashr_i32 s29, s28, 31
	s_lshl_b64 s[0:1], s[28:29], 12
	v_lshl_add_u64 v[2:3], v[112:113], 0, s[0:1]
	global_load_dwordx4 v[38:41], v[2:3], off nt
	global_load_dwordx4 v[26:29], v[2:3], off offset:1024 nt
	global_load_dwordx4 v[14:17], v[2:3], off offset:2048 nt
	s_nop 0
	global_load_dwordx4 v[2:5], v[2:3], off offset:3072 nt
	s_waitcnt vmcnt(28)
	v_and_b32_e32 v10, 64, v116
	v_xor_b32_e32 v11, 1, v116
	s_waitcnt vmcnt(18)
	v_add_u32_e32 v52, 64, v10
	v_xor_b32_e32 v12, 2, v116
	v_cmp_lt_i32_e32 vcc, v11, v52
	s_or_b32 s14, s60, 2
	v_xor_b32_e32 v13, 4, v116
	v_cndmask_b32_e32 v23, v116, v11, vcc
	v_cmp_lt_i32_e32 vcc, v12, v52
	v_xor_b32_e32 v22, 8, v116
	s_ashr_i32 s15, s14, 31
	v_cndmask_b32_e32 v12, v116, v12, vcc
	v_cmp_lt_i32_e32 vcc, v13, v52
	s_lshl_b64 s[2:3], s[14:15], 12
	v_lshl_add_u64 v[10:11], v[112:113], 0, s[2:3]
	v_cndmask_b32_e32 v13, v116, v13, vcc
	v_cmp_lt_i32_e32 vcc, v22, v52
	s_waitcnt vmcnt(14)
	v_lshlrev_b32_e32 v69, 2, v23
	v_lshlrev_b32_e32 v68, 2, v12
	v_cndmask_b32_e32 v22, v116, v22, vcc
	v_lshlrev_b32_e32 v67, 2, v13
	v_lshlrev_b32_e32 v66, 2, v22
	global_load_dwordx4 v[46:49], v[10:11], off nt
	global_load_dwordx4 v[34:37], v[10:11], off offset:1024 nt
	global_load_dwordx4 v[22:25], v[10:11], off offset:2048 nt
	s_nop 0
	global_load_dwordx4 v[10:13], v[10:11], off offset:3072 nt
	v_xor_b32_e32 v50, 16, v116
	v_cmp_lt_i32_e32 vcc, v50, v52
	v_xor_b32_e32 v51, 32, v116
	s_or_b32 s0, s60, 3
	v_cndmask_b32_e32 v50, v116, v50, vcc
	s_waitcnt vmcnt(16)
	v_lshlrev_b32_e32 v74, 2, v50
	v_cmp_lt_i32_e32 vcc, v51, v52
	s_ashr_i32 s1, s0, 31
	s_lshl_b64 s[2:3], s[0:1], 12
	v_cndmask_b32_e32 v51, v116, v51, vcc
	v_lshlrev_b32_e32 v75, 2, v51
	s_lshl_b64 s[0:1], s[0:1], 10
	s_waitcnt vmcnt(11)
	v_mul_f32_e32 v53, v43, v43
	v_mul_f32_e32 v54, v45, v45
	s_waitcnt vmcnt(10)
	v_mul_f32_e32 v55, v31, v31
	v_mul_f32_e32 v56, v33, v33
	s_waitcnt vmcnt(9)
	v_mul_f32_e32 v57, v19, v19
	v_mul_f32_e32 v58, v21, v21
	v_fmac_f32_e32 v53, v42, v42
	v_fmac_f32_e32 v54, v44, v44
	v_fmac_f32_e32 v55, v30, v30
	v_fmac_f32_e32 v56, v32, v32
	s_waitcnt vmcnt(8)
	v_mul_f32_e32 v59, v7, v7
	v_mul_f32_e32 v60, v9, v9
	v_fmac_f32_e32 v57, v18, v18
	v_fmac_f32_e32 v58, v20, v20
	v_add_f32_e32 v53, v53, v54
	v_add_f32_e32 v54, v55, v56
	v_fmac_f32_e32 v59, v6, v6
	v_fmac_f32_e32 v60, v8, v8
	v_add_f32_e32 v55, v57, v58
	v_add_f32_e32 v53, v53, v54
	v_add_f32_e32 v56, v59, v60
	v_add_f32_e32 v53, v53, v55
	v_add_f32_e32 v53, v53, v56
	ds_bpermute_b32 v54, v69, v53
	s_waitcnt vmcnt(7)
	v_mul_f32_e32 v61, v39, v39
	v_mul_f32_e32 v62, v41, v41
	s_waitcnt vmcnt(6)
	v_mul_f32_e32 v63, v27, v27
	v_mul_f32_e32 v64, v29, v29
	s_waitcnt lgkmcnt(0)
	v_add_f32_e32 v53, v53, v54
	ds_bpermute_b32 v54, v68, v53
	s_waitcnt vmcnt(5)
	v_mul_f32_e32 v65, v15, v15
	v_mul_f32_e32 v70, v17, v17
	v_fmac_f32_e32 v61, v38, v38
	v_fmac_f32_e32 v62, v40, v40
	s_waitcnt lgkmcnt(0)
	v_add_f32_e32 v53, v53, v54
	ds_bpermute_b32 v54, v67, v53
	v_fmac_f32_e32 v63, v26, v26
	v_fmac_f32_e32 v64, v28, v28
	s_waitcnt vmcnt(4)
	v_mul_f32_e32 v71, v3, v3
	v_mul_f32_e32 v72, v5, v5
	v_fmac_f32_e32 v65, v14, v14
	v_fmac_f32_e32 v70, v16, v16
	v_add_f32_e32 v55, v61, v62
	v_add_f32_e32 v56, v63, v64
	v_fmac_f32_e32 v71, v2, v2
	v_fmac_f32_e32 v72, v4, v4
	v_add_f32_e32 v57, v65, v70
	v_add_f32_e32 v55, v55, v56
	s_waitcnt lgkmcnt(0)
	v_add_f32_e32 v53, v53, v54
	v_add_f32_e32 v58, v71, v72
	v_add_f32_e32 v55, v55, v57
	ds_bpermute_b32 v54, v66, v53
	v_add_f32_e32 v55, v55, v58
	ds_bpermute_b32 v56, v69, v55
	s_waitcnt vmcnt(3)
	v_mul_f32_e32 v80, v47, v47
	v_mul_f32_e32 v81, v49, v49
	s_waitcnt lgkmcnt(1)
	v_add_f32_e32 v53, v53, v54
	ds_bpermute_b32 v54, v74, v53
	s_waitcnt lgkmcnt(1)
	v_add_f32_e32 v50, v55, v56
	ds_bpermute_b32 v55, v68, v50
	v_fmac_f32_e32 v80, v46, v46
	v_fmac_f32_e32 v81, v48, v48
	s_waitcnt lgkmcnt(1)
	v_add_f32_e32 v53, v53, v54
	ds_bpermute_b32 v54, v75, v53
	s_waitcnt lgkmcnt(1)
	v_add_f32_e32 v52, v50, v55
	ds_bpermute_b32 v55, v67, v52
	v_lshl_add_u64 v[50:51], v[112:113], 0, s[2:3]
	global_load_dwordx4 v[62:65], v[50:51], off nt
	global_load_dwordx4 v[58:61], v[50:51], off offset:1024 nt
	s_waitcnt lgkmcnt(1)
	v_add_f32_e32 v53, v53, v54
	v_fmamk_f32 v53, v53, 0x3a800000, v107
	s_waitcnt lgkmcnt(0)
	v_add_f32_e32 v52, v52, v55
	v_mul_f32_e32 v54, 0x4f800000, v53
	v_cmp_gt_f32_e32 vcc, s92, v53
	ds_bpermute_b32 v55, v66, v52
	v_add_f32_e32 v80, v80, v81
	v_cndmask_b32_e32 v53, v53, v54, vcc
	v_sqrt_f32_e32 v54, v53
	s_waitcnt vmcnt(4)
	v_mul_f32_e32 v81, v35, v35
	s_waitcnt lgkmcnt(0)
	v_add_f32_e32 v70, v52, v55
	v_mul_f32_e32 v82, v37, v37
	v_add_u32_e32 v52, -1, v54
	v_add_u32_e32 v55, 1, v54
	v_fma_f32 v56, -v52, v54, v53
	v_fma_f32 v57, -v55, v54, v53
	v_cmp_ge_f32_e64 s[4:5], 0, v56
	ds_bpermute_b32 v76, v74, v70
	v_fmac_f32_e32 v81, v34, v34
	v_cndmask_b32_e64 v52, v54, v52, s[4:5]
	v_cmp_lt_f32_e64 s[4:5], 0, v57
	v_fmac_f32_e32 v82, v36, v36
	v_add_f32_e32 v81, v81, v82
	v_cndmask_b32_e64 v52, v52, v55, s[4:5]
	v_mul_f32_e32 v54, 0x37800000, v52
	v_cndmask_b32_e32 v52, v52, v54, vcc
	v_cmp_class_f32_e32 vcc, v53, v109
	v_add_f32_e32 v80, v80, v81
	s_waitcnt vmcnt(3)
	v_mul_f32_e32 v81, v23, v23
	v_cndmask_b32_e32 v71, v52, v53, vcc
	global_load_dwordx4 v[54:57], v[50:51], off offset:2048 nt
	s_nop 0
	global_load_dwordx4 v[50:53], v[50:51], off offset:3072 nt
	v_mul_f32_e32 v82, v25, v25
	v_fmac_f32_e32 v81, v22, v22
	v_fmac_f32_e32 v82, v24, v24
	v_add_f32_e32 v81, v81, v82
	s_waitcnt lgkmcnt(0)
	v_add_f32_e32 v70, v70, v76
	v_add_f32_e32 v80, v80, v81
	s_waitcnt vmcnt(4)
	v_mul_f32_e32 v81, v11, v11
	v_mul_f32_e32 v82, v13, v13
	ds_bpermute_b32 v76, v75, v70
	v_fmac_f32_e32 v81, v10, v10
	v_fmac_f32_e32 v82, v12, v12
	v_add_f32_e32 v81, v81, v82
	v_add_f32_e32 v80, v80, v81
	v_div_scale_f32 v72, s[2:3], v71, v71, 1.0
	ds_bpermute_b32 v81, v69, v80
	v_rcp_f32_e32 v73, v72
	s_waitcnt lgkmcnt(1)
	v_add_f32_e32 v70, v70, v76
	v_fmamk_f32 v70, v70, 0x3a800000, v107
	v_mul_f32_e32 v76, 0x4f800000, v70
	v_cmp_gt_f32_e64 s[4:5], s92, v70
	v_fma_f32 v77, -v72, v73, 1.0
	s_waitcnt lgkmcnt(0)
	v_add_f32_e32 v80, v80, v81
	v_cndmask_b32_e64 v70, v70, v76, s[4:5]
	v_fmac_f32_e32 v73, v77, v73
	v_div_scale_f32 v77, vcc, 1.0, v71, 1.0
	v_sqrt_f32_e32 v76, v70
	ds_bpermute_b32 v81, v68, v80
	v_mul_f32_e32 v78, v77, v73
	v_fma_f32 v79, -v72, v78, v77
	v_fmac_f32_e32 v78, v79, v73
	v_fma_f32 v72, -v72, v78, v77
	v_add_u32_e32 v77, -1, v76
	v_fma_f32 v79, -v77, v76, v70
	s_waitcnt lgkmcnt(0)
	v_add_f32_e32 v80, v80, v81
	v_cmp_ge_f32_e64 s[8:9], 0, v79
	v_add_u32_e32 v79, 1, v76
	ds_bpermute_b32 v81, v67, v80
	v_cndmask_b32_e64 v77, v76, v77, s[8:9]
	v_fma_f32 v76, -v79, v76, v70
	v_cmp_lt_f32_e64 s[8:9], 0, v76
	v_div_fmas_f32 v72, v72, v73, v78
	v_div_fixup_f32 v78, v72, v71, 1.0
	v_cndmask_b32_e64 v76, v77, v79, s[8:9]
	v_mul_f32_e32 v77, 0x37800000, v76
	v_cndmask_b32_e64 v76, v76, v77, s[4:5]
	s_waitcnt lgkmcnt(0)
	v_add_f32_e32 v77, v80, v81
	ds_bpermute_b32 v79, v66, v77
	v_cmp_class_f32_e64 s[4:5], v70, v109
	s_waitcnt vmcnt(2)
	v_mul_f32_e32 v72, v61, v61
	v_fmac_f32_e32 v72, v60, v60
	v_cndmask_b32_e64 v76, v76, v70, s[4:5]
	s_waitcnt lgkmcnt(0)
	v_add_f32_e32 v70, v77, v79
	v_div_scale_f32 v80, s[2:3], v76, v76, 1.0
	ds_bpermute_b32 v77, v74, v70
	v_rcp_f32_e32 v81, v80
	v_mul_f32_e32 v42, v42, v78
	v_mul_f32_e32 v43, v43, v78
	v_mul_f32_e32 v44, v44, v78
	v_fma_f32 v71, -v80, v81, 1.0
	s_waitcnt lgkmcnt(0)
	v_add_f32_e32 v70, v70, v77
	v_fmac_f32_e32 v81, v71, v81
	ds_bpermute_b32 v71, v75, v70
	v_div_scale_f32 v77, vcc, 1.0, v76, 1.0
	v_mul_f32_e32 v79, v77, v81
	v_fma_f32 v82, -v80, v79, v77
	s_waitcnt lgkmcnt(0)
	v_add_f32_e32 v70, v70, v71
	v_fmamk_f32 v70, v70, 0x3a800000, v107
	v_mul_f32_e32 v71, 0x4f800000, v70
	v_cmp_gt_f32_e64 s[4:5], s92, v70
	v_fmac_f32_e32 v79, v82, v81
	v_fma_f32 v77, -v80, v79, v77
	v_cndmask_b32_e64 v83, v70, v71, s[4:5]
	v_mul_f32_e32 v70, v63, v63
	v_mul_f32_e32 v71, v65, v65
	v_fmac_f32_e32 v70, v62, v62
	v_fmac_f32_e32 v71, v64, v64
	v_add_f32_e32 v70, v70, v71
	v_mul_f32_e32 v71, v59, v59
	v_fmac_f32_e32 v71, v58, v58
	v_add_f32_e32 v71, v71, v72
	v_add_f32_e32 v70, v70, v71
	s_waitcnt vmcnt(1)
	v_mul_f32_e32 v71, v55, v55
	v_mul_f32_e32 v72, v57, v57
	v_fmac_f32_e32 v71, v54, v54
	v_fmac_f32_e32 v72, v56, v56
	v_add_f32_e32 v71, v71, v72
	v_add_f32_e32 v85, v70, v71
	v_mov_b64_e32 v[70:71], v[140:141]
	v_mov_b64_e32 v[72:73], v[142:143]
	s_waitcnt vmcnt(0)
	v_mul_f32_e32 v86, v51, v51
	v_mul_f32_e32 v87, v53, v53
	v_fmac_f32_e32 v86, v50, v50
	v_fmac_f32_e32 v87, v52, v52
	v_add_f32_e32 v86, v86, v87
	v_add_f32_e32 v85, v85, v86
	ds_bpermute_b32 v69, v69, v85
	v_sqrt_f32_e32 v84, v83
	v_mul_f32_e32 v30, v30, v78
	v_mul_f32_e32 v31, v31, v78
	v_mul_f32_e32 v32, v32, v78
	s_waitcnt lgkmcnt(0)
	v_add_f32_e32 v69, v85, v69
	ds_bpermute_b32 v68, v68, v69
	v_add_u32_e32 v80, -1, v84
	v_fma_f32 v82, -v80, v84, v83
	v_cmp_ge_f32_e64 s[8:9], 0, v82
	v_add_u32_e32 v82, 1, v84
	s_waitcnt lgkmcnt(0)
	v_add_f32_e32 v68, v69, v68
	ds_bpermute_b32 v67, v67, v68
	v_cndmask_b32_e64 v80, v84, v80, s[8:9]
	v_fma_f32 v84, -v82, v84, v83
	v_cmp_lt_f32_e64 s[8:9], 0, v84
	v_mul_f32_e32 v18, v18, v78
	s_waitcnt lgkmcnt(0)
	v_add_f32_e32 v67, v68, v67
	ds_bpermute_b32 v66, v66, v67
	v_cndmask_b32_e64 v69, v80, v82, s[8:9]
	v_mul_f32_e32 v80, 0x37800000, v69
	v_cndmask_b32_e64 v69, v69, v80, s[4:5]
	v_cmp_class_f32_e64 s[4:5], v83, v109
	s_waitcnt lgkmcnt(0)
	v_add_f32_e32 v66, v67, v66
	ds_bpermute_b32 v67, v74, v66
	v_cndmask_b32_e64 v68, v69, v83, s[4:5]
	v_div_scale_f32 v69, s[2:3], v68, v68, 1.0
	v_rcp_f32_e32 v80, v69
	s_waitcnt lgkmcnt(0)
	v_add_f32_e32 v66, v66, v67
	ds_bpermute_b32 v67, v75, v66
	v_div_fmas_f32 v74, v77, v81, v79
	v_div_fixup_f32 v74, v74, v76, 1.0
	v_fma_f32 v76, -v69, v80, 1.0
	v_fmac_f32_e32 v80, v76, v80
	s_waitcnt lgkmcnt(0)
	v_add_f32_e32 v66, v66, v67
	v_fmamk_f32 v66, v66, 0x3a800000, v107
	v_mul_f32_e32 v67, 0x4f800000, v66
	v_cmp_gt_f32_e64 s[4:5], s92, v66
	v_div_scale_f32 v75, vcc, 1.0, v68, 1.0
	s_nop 0
	v_cndmask_b32_e64 v66, v66, v67, s[4:5]
	v_sqrt_f32_e32 v67, v66
	v_mul_f32_e32 v76, v75, v80
	v_fma_f32 v77, -v69, v76, v75
	v_fmac_f32_e32 v76, v77, v80
	v_fma_f32 v69, -v69, v76, v75
	v_add_u32_e32 v75, -1, v67
	v_fma_f32 v77, -v75, v67, v66
	v_cmp_ge_f32_e64 s[8:9], 0, v77
	v_add_u32_e32 v77, 1, v67
	v_div_fmas_f32 v69, v69, v80, v76
	v_cndmask_b32_e64 v75, v67, v75, s[8:9]
	v_fma_f32 v67, -v77, v67, v66
	v_cmp_lt_f32_e64 s[8:9], 0, v67
	v_div_fixup_f32 v68, v69, v68, 1.0
	v_mul_f32_e32 v38, v38, v74
	v_cndmask_b32_e64 v67, v75, v77, s[8:9]
	v_mul_f32_e32 v75, 0x37800000, v67
	v_cndmask_b32_e64 v67, v67, v75, s[4:5]
	v_cmp_class_f32_e64 s[4:5], v66, v109
	v_mul_f32_e32 v39, v39, v74
	v_mul_f32_e32 v40, v40, v74
	v_cndmask_b32_e64 v66, v67, v66, s[4:5]
	v_div_scale_f32 v67, s[2:3], v66, v66, 1.0
	v_rcp_f32_e32 v75, v67
	s_lshl_b64 s[2:3], s[60:61], 10
	v_mul_f32_e32 v26, v26, v74
	v_mul_f32_e32 v27, v27, v74
	v_fma_f32 v69, -v67, v75, 1.0
	v_fmac_f32_e32 v75, v69, v75
	v_div_scale_f32 v69, vcc, 1.0, v66, 1.0
	v_mul_f32_e32 v76, v69, v75
	v_fma_f32 v77, -v67, v76, v69
	v_fmac_f32_e32 v76, v77, v75
	v_fma_f32 v67, -v67, v76, v69
	s_waitcnt vmcnt(0)
	v_mul_f32_e32 v38, v38, v70
	v_mul_f32_e32 v39, v39, v71
	v_mov_b32_e32 v69, v101
	v_cvt_pk_fp8_f32 v69, v38, v39
	v_mul_f32_e32 v39, v41, v74
	v_mul_f32_e32 v38, v40, v72
	v_mul_f32_e32 v39, v39, v73
	v_cvt_pk_fp8_f32 v69, v38, v39 op_sel:[0,0,1]
	v_mul_f32_e32 v38, v46, v68
	v_mul_f32_e32 v39, v47, v68
	v_mul_f32_e32 v38, v38, v70
	v_mul_f32_e32 v39, v39, v71
	v_mov_b32_e32 v41, v101
	v_cvt_pk_fp8_f32 v41, v38, v39
	v_div_fmas_f32 v67, v67, v75, v76
	v_mul_f32_e32 v40, v48, v68
	v_mul_f32_e32 v39, v49, v68
	v_div_fixup_f32 v66, v67, v66, 1.0
	v_mul_f32_e32 v38, v40, v72
	v_mul_f32_e32 v39, v39, v73
	v_cvt_pk_fp8_f32 v41, v38, v39 op_sel:[0,0,1]
	v_mul_f32_e32 v38, v62, v66
	v_mul_f32_e32 v39, v63, v66
	v_mul_f32_e32 v42, v42, v70
	v_mul_f32_e32 v43, v43, v71
	v_mov_b32_e32 v67, v101
	v_mul_f32_e32 v38, v70, v38
	v_mul_f32_e32 v39, v71, v39
	v_mov_b32_e32 v62, v101
	v_cvt_pk_fp8_f32 v67, v42, v43
	v_cvt_pk_fp8_f32 v62, v38, v39
	v_mul_f32_e32 v43, v45, v78
	v_mul_f32_e32 v40, v64, v66
	v_mul_f32_e32 v39, v65, v66
	v_mul_f32_e32 v42, v44, v72
	v_mul_f32_e32 v43, v43, v73
	v_mul_f32_e32 v38, v72, v40
	v_mul_f32_e32 v39, v73, v39
	v_cvt_pk_fp8_f32 v67, v42, v43 op_sel:[0,0,1]
	v_cvt_pk_fp8_f32 v62, v38, v39 op_sel:[0,0,1]
	v_lshl_add_u64 v[42:43], v[114:115], 0, s[2:3]
	s_lshl_b64 s[2:3], s[28:29], 10
	v_lshl_add_u64 v[44:45], v[114:115], 0, s[2:3]
	s_lshl_b64 s[2:3], s[14:15], 10
	v_lshl_add_u64 v[46:47], v[114:115], 0, s[2:3]
	v_lshl_add_u64 v[48:49], v[114:115], 0, s[0:1]
	global_store_dword v[42:43], v67, off
	global_store_dword v[44:45], v69, off
	global_store_dword v[46:47], v41, off
	global_store_dword v[48:49], v62, off
	s_nop 0
	v_mov_b64_e32 v[38:39], v[144:145]
	v_mov_b64_e32 v[40:41], v[146:147]
	v_mov_b32_e32 v62, v101
	v_mul_f32_e32 v28, v28, v74
	v_mul_f32_e32 v19, v19, v78
	v_mul_f32_e32 v20, v20, v78
	v_mul_f32_e32 v14, v14, v74
	v_mul_f32_e32 v15, v15, v74
	v_mul_f32_e32 v16, v16, v74
	v_mul_f32_e32 v6, v6, v78
	v_mul_f32_e32 v7, v7, v78
	v_mul_f32_e32 v8, v8, v78
	v_mul_f32_e32 v2, v2, v74
	v_mul_f32_e32 v3, v3, v74
	v_mul_f32_e32 v4, v4, v74
	s_nop 0
	v_mul_f32_e32 v30, v30, v38
	v_mul_f32_e32 v31, v31, v39
	v_cvt_pk_fp8_f32 v62, v30, v31
	v_mul_f32_e32 v31, v33, v78
	v_mul_f32_e32 v30, v32, v40
	v_mul_f32_e32 v31, v31, v41
	v_cvt_pk_fp8_f32 v62, v30, v31 op_sel:[0,0,1]
	v_mul_f32_e32 v26, v26, v38
	v_mul_f32_e32 v27, v27, v39
	v_mov_b32_e32 v30, v101
	v_cvt_pk_fp8_f32 v30, v26, v27
	v_mul_f32_e32 v27, v29, v74
	v_mul_f32_e32 v26, v28, v40
	v_mul_f32_e32 v27, v27, v41
	v_cvt_pk_fp8_f32 v30, v26, v27 op_sel:[0,0,1]
	v_mul_f32_e32 v26, v34, v68
	v_mul_f32_e32 v27, v35, v68
	v_mul_f32_e32 v26, v26, v38
	v_mul_f32_e32 v27, v27, v39
	v_mov_b32_e32 v29, v101
	v_cvt_pk_fp8_f32 v29, v26, v27
	v_mul_f32_e32 v28, v36, v68
	v_mul_f32_e32 v27, v37, v68
	v_mul_f32_e32 v26, v28, v40
	v_mul_f32_e32 v27, v27, v41
	v_cvt_pk_fp8_f32 v29, v26, v27 op_sel:[0,0,1]
	v_mul_f32_e32 v26, v58, v66
	v_mul_f32_e32 v27, v59, v66
	v_mul_f32_e32 v26, v26, v38
	v_mul_f32_e32 v27, v27, v39
	v_mov_b32_e32 v31, v101
	v_cvt_pk_fp8_f32 v31, v26, v27
	v_mul_f32_e32 v28, v60, v66
	v_mul_f32_e32 v27, v61, v66
	v_mul_f32_e32 v26, v28, v40
	v_mul_f32_e32 v27, v27, v41
	v_cvt_pk_fp8_f32 v31, v26, v27 op_sel:[0,0,1]
	global_store_dword v[42:43], v62, off offset:256
	global_store_dword v[44:45], v30, off offset:256
	global_store_dword v[46:47], v29, off offset:256
	global_store_dword v[48:49], v31, off offset:256
	s_nop 0
	v_mov_b64_e32 v[26:27], v[148:149]
	v_mov_b64_e32 v[28:29], v[150:151]
	v_mov_b32_e32 v30, v101
	s_nop 0
	v_mul_f32_e32 v18, v18, v26
	v_mul_f32_e32 v19, v19, v27
	v_cvt_pk_fp8_f32 v30, v18, v19
	v_mul_f32_e32 v19, v21, v78
	v_mul_f32_e32 v18, v20, v28
	v_mul_f32_e32 v19, v19, v29
	v_cvt_pk_fp8_f32 v30, v18, v19 op_sel:[0,0,1]
	v_mul_f32_e32 v14, v14, v26
	v_mul_f32_e32 v15, v15, v27
	v_mov_b32_e32 v18, v101
	v_cvt_pk_fp8_f32 v18, v14, v15
	v_mul_f32_e32 v15, v17, v74
	v_mul_f32_e32 v14, v16, v28
	v_mul_f32_e32 v15, v15, v29
	v_cvt_pk_fp8_f32 v18, v14, v15 op_sel:[0,0,1]
	v_mul_f32_e32 v14, v22, v68
	v_mul_f32_e32 v15, v23, v68
	v_mul_f32_e32 v14, v14, v26
	v_mul_f32_e32 v15, v15, v27
	v_mov_b32_e32 v17, v101
	v_cvt_pk_fp8_f32 v17, v14, v15
	v_mul_f32_e32 v16, v24, v68
	v_mul_f32_e32 v15, v25, v68
	v_mul_f32_e32 v14, v16, v28
	v_mul_f32_e32 v15, v15, v29
	v_cvt_pk_fp8_f32 v17, v14, v15 op_sel:[0,0,1]
	v_mul_f32_e32 v14, v54, v66
	v_mul_f32_e32 v15, v55, v66
	v_mul_f32_e32 v14, v14, v26
	v_mul_f32_e32 v15, v15, v27
	v_mov_b32_e32 v19, v101
	v_cvt_pk_fp8_f32 v19, v14, v15
	v_mul_f32_e32 v16, v56, v66
	v_mul_f32_e32 v15, v57, v66
	v_mul_f32_e32 v14, v16, v28
	v_mul_f32_e32 v15, v15, v29
	v_cvt_pk_fp8_f32 v19, v14, v15 op_sel:[0,0,1]
	global_store_dword v[42:43], v30, off offset:512
	global_store_dword v[44:45], v18, off offset:512
	global_store_dword v[46:47], v17, off offset:512
	global_store_dword v[48:49], v19, off offset:512
	s_nop 0
	v_mov_b64_e32 v[14:15], v[152:153]
	v_mov_b64_e32 v[16:17], v[154:155]
	v_mov_b32_e32 v18, v101
	s_nop 0
	v_mul_f32_e32 v6, v6, v14
	v_mul_f32_e32 v7, v7, v15
	v_cvt_pk_fp8_f32 v18, v6, v7
	v_mul_f32_e32 v7, v9, v78
	v_mul_f32_e32 v6, v8, v16
	v_mul_f32_e32 v7, v7, v17
	v_cvt_pk_fp8_f32 v18, v6, v7 op_sel:[0,0,1]
	v_mul_f32_e32 v2, v2, v14
	v_mul_f32_e32 v3, v3, v15
	v_mov_b32_e32 v6, v101
	v_cvt_pk_fp8_f32 v6, v2, v3
	v_mul_f32_e32 v3, v5, v74
	v_mul_f32_e32 v2, v4, v16
	v_mul_f32_e32 v3, v3, v17
	v_cvt_pk_fp8_f32 v6, v2, v3 op_sel:[0,0,1]
	v_mul_f32_e32 v2, v10, v68
	v_mul_f32_e32 v3, v11, v68
	v_mul_f32_e32 v2, v2, v14
	v_mul_f32_e32 v3, v3, v15
	v_mov_b32_e32 v5, v101
	v_cvt_pk_fp8_f32 v5, v2, v3
	v_mul_f32_e32 v4, v12, v68
	v_mul_f32_e32 v3, v13, v68
	v_mul_f32_e32 v2, v4, v16
	v_mul_f32_e32 v3, v3, v17
	v_cvt_pk_fp8_f32 v5, v2, v3 op_sel:[0,0,1]
	v_mul_f32_e32 v2, v50, v66
	v_mul_f32_e32 v3, v51, v66
	v_mul_f32_e32 v2, v2, v14
	v_mul_f32_e32 v3, v3, v15
	v_mov_b32_e32 v7, v101
	v_cvt_pk_fp8_f32 v7, v2, v3
	v_mul_f32_e32 v4, v52, v66
	v_mul_f32_e32 v3, v53, v66
	v_mul_f32_e32 v2, v4, v16
	v_mul_f32_e32 v3, v3, v17
	v_cvt_pk_fp8_f32 v7, v2, v3 op_sel:[0,0,1]
	global_store_dword v[42:43], v18, off offset:768
	global_store_dword v[44:45], v6, off offset:768
	global_store_dword v[46:47], v5, off offset:768
	global_store_dword v[48:49], v7, off offset:768
